# s16
# baseline (speedup 1.0000x reference)
.LBB1_14:
	s_or_b64 exec, exec, s[0:1]
	v_readfirstlane_b32 s100, v0
	s_nop 3
	s_cmp_lt_u32 s100, 0x100
	s_cbranch_scc1 .Lpf_0_a
	s_setprio 1
	s_branch .Lpf_0_b
.Lpf_0_a:
	s_setprio 0
.Lpf_0_b:
	s_cmp_lg_u32 s2, 0x1800000
	s_cselect_b32 s32, 0x800000, 0
	s_add_u32 s100, s22, s32
	s_addc_u32 s101, s90, 0
	global_load_dwordx4 v[216:219], v201, s[100:101] nt
	s_add_u32 s100, s22, s32
	s_addc_u32 s101, s90, 0
	s_add_u32 s100, s100, 0x20000
	s_addc_u32 s101, s101, 0
	global_load_dwordx4 v[220:223], v201, s[100:101] nt
	s_add_u32 s100, s22, s32
	s_addc_u32 s101, s90, 0
	s_add_u32 s100, s100, 0x40000
	s_addc_u32 s101, s101, 0
	global_load_dwordx4 v[224:227], v201, s[100:101] nt
	s_add_u32 s100, s22, s32
	s_addc_u32 s101, s90, 0
	s_add_u32 s100, s100, 0x60000
	s_addc_u32 s101, s101, 0
	global_load_dwordx4 v[228:231], v201, s[100:101] nt
	s_add_u32 s100, s22, s32
	s_addc_u32 s101, s90, 0
	s_add_u32 s100, s100, 0x80000
	s_addc_u32 s101, s101, 0
	global_load_dwordx4 v[232:235], v201, s[100:101] nt
	s_add_u32 s100, s22, s32
	s_addc_u32 s101, s90, 0
	s_add_u32 s100, s100, 0xa0000
	s_addc_u32 s101, s101, 0
	global_load_dwordx4 v[236:239], v201, s[100:101] nt
	s_add_u32 s100, s22, s32
	s_addc_u32 s101, s90, 0
	s_add_u32 s100, s100, 0xc0000
	s_addc_u32 s101, s101, 0
	global_load_dwordx4 v[240:243], v201, s[100:101] nt
	s_add_u32 s100, s22, s32
	s_addc_u32 s101, s90, 0
	s_add_u32 s100, s100, 0xe0000
	s_addc_u32 s101, s101, 0
	global_load_dwordx4 v[244:247], v201, s[100:101] nt
	v_exp_f32_e32 v154, v154
	v_exp_f32_e32 v155, v155
	v_exp_f32_e32 v156, v156
	v_exp_f32_e32 v157, v157
	v_pk_add_f32 v[154:155], v[154:155], 1.0 op_sel_hi:[1,0]
	v_pk_add_f32 v[156:157], v[156:157], 1.0 op_sel_hi:[1,0]
	v_rcp_f32_e32 v154, v154
	v_rcp_f32_e32 v155, v155
	v_rcp_f32_e32 v156, v156
	v_rcp_f32_e32 v157, v157
	v_pk_mul_f32 v[248:249], v[154:155], v[90:91]
	v_pk_fma_f32 v[248:249], v[156:157], v[92:93], v[248:249]
	v_exp_f32_e32 v158, v158
	v_exp_f32_e32 v159, v159
	v_exp_f32_e32 v160, v160
	v_exp_f32_e32 v161, v161
	v_pk_add_f32 v[158:159], v[158:159], 1.0 op_sel_hi:[1,0]
	v_pk_add_f32 v[160:161], v[160:161], 1.0 op_sel_hi:[1,0]
	v_rcp_f32_e32 v158, v158
	v_rcp_f32_e32 v159, v159
	v_rcp_f32_e32 v160, v160
	v_rcp_f32_e32 v161, v161
	v_pk_fma_f32 v[248:249], v[158:159], v[102:103], v[248:249]
	v_pk_fma_f32 v[248:249], v[160:161], v[104:105], v[248:249]
	v_exp_f32_e32 v166, v166
	v_exp_f32_e32 v167, v167
	v_exp_f32_e32 v168, v168
	v_exp_f32_e32 v169, v169
	v_pk_add_f32 v[166:167], v[166:167], 1.0 op_sel_hi:[1,0]
	v_pk_add_f32 v[168:169], v[168:169], 1.0 op_sel_hi:[1,0]
	v_rcp_f32_e32 v166, v166
	v_rcp_f32_e32 v167, v167
	v_rcp_f32_e32 v168, v168
	v_rcp_f32_e32 v169, v169
	v_pk_fma_f32 v[248:249], v[166:167], v[86:87], v[248:249]
	v_pk_fma_f32 v[248:249], v[168:169], v[88:89], v[248:249]
	v_exp_f32_e32 v170, v170
	v_exp_f32_e32 v171, v171
	v_exp_f32_e32 v172, v172
	v_exp_f32_e32 v173, v173
	v_pk_add_f32 v[170:171], v[170:171], 1.0 op_sel_hi:[1,0]
	v_pk_add_f32 v[172:173], v[172:173], 1.0 op_sel_hi:[1,0]
	v_rcp_f32_e32 v170, v170
	v_rcp_f32_e32 v171, v171
	v_rcp_f32_e32 v172, v172
	v_rcp_f32_e32 v173, v173
	v_pk_fma_f32 v[248:249], v[170:171], v[98:99], v[248:249]
	v_pk_fma_f32 v[248:249], v[172:173], v[100:101], v[248:249]
	v_exp_f32_e32 v178, v178
	v_exp_f32_e32 v179, v179
	v_exp_f32_e32 v180, v180
	v_exp_f32_e32 v181, v181
	v_pk_add_f32 v[178:179], v[178:179], 1.0 op_sel_hi:[1,0]
	v_pk_add_f32 v[180:181], v[180:181], 1.0 op_sel_hi:[1,0]
	v_rcp_f32_e32 v178, v178
	v_rcp_f32_e32 v179, v179
	v_rcp_f32_e32 v180, v180
	v_rcp_f32_e32 v181, v181
	v_pk_fma_f32 v[248:249], v[178:179], v[118:119], v[248:249]
	v_pk_fma_f32 v[248:249], v[180:181], v[120:121], v[248:249]
	v_exp_f32_e32 v182, v182
	v_exp_f32_e32 v183, v183
	v_exp_f32_e32 v184, v184
	v_exp_f32_e32 v185, v185
	v_pk_add_f32 v[182:183], v[182:183], 1.0 op_sel_hi:[1,0]
	v_pk_add_f32 v[184:185], v[184:185], 1.0 op_sel_hi:[1,0]
	v_rcp_f32_e32 v182, v182
	v_rcp_f32_e32 v183, v183
	v_rcp_f32_e32 v184, v184
	v_rcp_f32_e32 v185, v185
	v_pk_fma_f32 v[248:249], v[182:183], v[110:111], v[248:249]
	v_pk_fma_f32 v[248:249], v[184:185], v[112:113], v[248:249]
	v_exp_f32_e32 v186, v186
	v_exp_f32_e32 v187, v187
	v_exp_f32_e32 v188, v188
	v_exp_f32_e32 v189, v189
	v_pk_add_f32 v[186:187], v[186:187], 1.0 op_sel_hi:[1,0]
	v_pk_add_f32 v[188:189], v[188:189], 1.0 op_sel_hi:[1,0]
	v_rcp_f32_e32 v186, v186
	v_rcp_f32_e32 v187, v187
	v_rcp_f32_e32 v188, v188
	v_rcp_f32_e32 v189, v189
	v_pk_fma_f32 v[248:249], v[186:187], v[126:127], v[248:249]
	v_pk_fma_f32 v[248:249], v[188:189], v[128:129], v[248:249]
	v_exp_f32_e32 v190, v190
	v_exp_f32_e32 v191, v191
	v_exp_f32_e32 v192, v192
	v_exp_f32_e32 v193, v193
	v_pk_add_f32 v[190:191], v[190:191], 1.0 op_sel_hi:[1,0]
	v_pk_add_f32 v[192:193], v[192:193], 1.0 op_sel_hi:[1,0]
	v_rcp_f32_e32 v190, v190
	v_rcp_f32_e32 v191, v191
	v_rcp_f32_e32 v192, v192
	v_rcp_f32_e32 v193, v193
	v_pk_fma_f32 v[248:249], v[190:191], v[122:123], v[248:249]
	v_pk_fma_f32 v[248:249], v[192:193], v[124:125], v[248:249]
	v_add_f32_e32 v158, v248, v249
	ds_bpermute_b32 v154, v206, v158
	s_waitcnt vmcnt(10)
	v_cmp_eq_u32_e64 s[0:1], 0, v211
	s_waitcnt lgkmcnt(0)
	v_add_f32_e32 v154, v158, v154
	ds_bpermute_b32 v155, v205, v154
	s_waitcnt lgkmcnt(0)
	v_add_f32_e32 v154, v154, v155
	v_add_f32_e32 v154, v212, v154
	v_mul_f32_e32 v154, 0x3fb8aa3b, v154
	v_exp_f32_e32 v154, v154
	s_nop 0
	v_cndmask_b32_e64 v154, 0, v154, s[0:1]
	s_and_saveexec_b64 s[0:1], vcc
	s_cbranch_execz .LBB1_16
	global_store_dword v[198:199], v154, off offset:64
.LBB1_16:
	s_or_b64 exec, exec, s[0:1]
	v_readfirstlane_b32 s100, v0
	s_nop 3
	s_cmp_lt_u32 s100, 0x100
	s_cbranch_scc1 .Lpf_1_a
	s_setprio 0
	s_branch .Lpf_1_b
.Lpf_1_a:
	s_setprio 1
.Lpf_1_b:
	s_add_u32 s100, s22, s32
	s_addc_u32 s101, s90, 0
	s_add_u32 s100, s100, 0x100
	s_addc_u32 s101, s101, 0
	global_load_dwordx4 v[156:159], v201, s[100:101] nt
	s_add_u32 s100, s22, s32
	s_addc_u32 s101, s90, 0
	s_add_u32 s100, s100, 0x20100
	s_addc_u32 s101, s101, 0
	global_load_dwordx4 v[168:171], v201, s[100:101] nt
	s_add_u32 s100, s22, s32
	s_addc_u32 s101, s90, 0
	s_add_u32 s100, s100, 0x40100
	s_addc_u32 s101, s101, 0
	global_load_dwordx4 v[180:183], v201, s[100:101] nt
	s_add_u32 s100, s22, s32
	s_addc_u32 s101, s90, 0
	s_add_u32 s100, s100, 0x60100
	s_addc_u32 s101, s101, 0
	global_load_dwordx4 v[184:187], v201, s[100:101] nt
	s_add_u32 s100, s22, s32
	s_addc_u32 s101, s90, 0
	s_add_u32 s100, s100, 0x80100
	s_addc_u32 s101, s101, 0
	global_load_dwordx4 v[188:191], v201, s[100:101] nt
	v_exp_f32_e32 v106, v106
	v_exp_f32_e32 v107, v107
	v_exp_f32_e32 v108, v108
	v_exp_f32_e32 v109, v109
	v_pk_add_f32 v[106:107], v[106:107], 1.0 op_sel_hi:[1,0]
	v_pk_add_f32 v[108:109], v[108:109], 1.0 op_sel_hi:[1,0]
	v_rcp_f32_e32 v106, v106
	v_rcp_f32_e32 v107, v107
	v_rcp_f32_e32 v108, v108
	v_rcp_f32_e32 v109, v109
	v_pk_mul_f32 v[248:249], v[106:107], v[90:91]
	v_pk_fma_f32 v[248:249], v[108:109], v[92:93], v[248:249]
	v_exp_f32_e32 v114, v114
	v_exp_f32_e32 v115, v115
	v_exp_f32_e32 v116, v116
	v_exp_f32_e32 v117, v117
	v_pk_add_f32 v[114:115], v[114:115], 1.0 op_sel_hi:[1,0]
	v_pk_add_f32 v[116:117], v[116:117], 1.0 op_sel_hi:[1,0]
	v_rcp_f32_e32 v114, v114
	v_rcp_f32_e32 v115, v115
	v_rcp_f32_e32 v116, v116
	v_rcp_f32_e32 v117, v117
	v_pk_fma_f32 v[248:249], v[114:115], v[102:103], v[248:249]
	v_pk_fma_f32 v[248:249], v[116:117], v[104:105], v[248:249]
	v_exp_f32_e32 v134, v134
	v_exp_f32_e32 v135, v135
	v_exp_f32_e32 v136, v136
	v_exp_f32_e32 v137, v137
	v_pk_add_f32 v[134:135], v[134:135], 1.0 op_sel_hi:[1,0]
	v_pk_add_f32 v[136:137], v[136:137], 1.0 op_sel_hi:[1,0]
	v_rcp_f32_e32 v134, v134
	v_rcp_f32_e32 v135, v135
	v_rcp_f32_e32 v136, v136
	v_rcp_f32_e32 v137, v137
	v_pk_fma_f32 v[248:249], v[134:135], v[86:87], v[248:249]
	v_pk_fma_f32 v[248:249], v[136:137], v[88:89], v[248:249]
	v_exp_f32_e32 v138, v138
	v_exp_f32_e32 v139, v139
	v_exp_f32_e32 v140, v140
	v_exp_f32_e32 v141, v141
	v_pk_add_f32 v[138:139], v[138:139], 1.0 op_sel_hi:[1,0]
	v_pk_add_f32 v[140:141], v[140:141], 1.0 op_sel_hi:[1,0]
	v_rcp_f32_e32 v138, v138
	v_rcp_f32_e32 v139, v139
	v_rcp_f32_e32 v140, v140
	v_rcp_f32_e32 v141, v141
	v_pk_fma_f32 v[248:249], v[138:139], v[98:99], v[248:249]
	v_pk_fma_f32 v[248:249], v[140:141], v[100:101], v[248:249]
	v_exp_f32_e32 v146, v146
	v_exp_f32_e32 v147, v147
	v_exp_f32_e32 v148, v148
	v_exp_f32_e32 v149, v149
	v_pk_add_f32 v[146:147], v[146:147], 1.0 op_sel_hi:[1,0]
	v_pk_add_f32 v[148:149], v[148:149], 1.0 op_sel_hi:[1,0]
	v_rcp_f32_e32 v146, v146
	v_rcp_f32_e32 v147, v147
	v_rcp_f32_e32 v148, v148
	v_rcp_f32_e32 v149, v149
	v_pk_fma_f32 v[248:249], v[146:147], v[118:119], v[248:249]
	v_pk_fma_f32 v[248:249], v[148:149], v[120:121], v[248:249]
	v_exp_f32_e32 v150, v150
	v_exp_f32_e32 v151, v151
	v_exp_f32_e32 v152, v152
	v_exp_f32_e32 v153, v153
	v_pk_add_f32 v[150:151], v[150:151], 1.0 op_sel_hi:[1,0]
	v_pk_add_f32 v[152:153], v[152:153], 1.0 op_sel_hi:[1,0]
	v_rcp_f32_e32 v150, v150
	v_rcp_f32_e32 v151, v151
	v_rcp_f32_e32 v152, v152
	v_rcp_f32_e32 v153, v153
	v_pk_fma_f32 v[248:249], v[150:151], v[110:111], v[248:249]
	v_pk_fma_f32 v[248:249], v[152:153], v[112:113], v[248:249]
	v_exp_f32_e32 v162, v162
	v_exp_f32_e32 v163, v163
	v_exp_f32_e32 v164, v164
	v_exp_f32_e32 v165, v165
	v_pk_add_f32 v[162:163], v[162:163], 1.0 op_sel_hi:[1,0]
	v_pk_add_f32 v[164:165], v[164:165], 1.0 op_sel_hi:[1,0]
	v_rcp_f32_e32 v162, v162
	v_rcp_f32_e32 v163, v163
	v_rcp_f32_e32 v164, v164
	v_rcp_f32_e32 v165, v165
	v_pk_fma_f32 v[248:249], v[162:163], v[126:127], v[248:249]
	v_pk_fma_f32 v[248:249], v[164:165], v[128:129], v[248:249]
	v_exp_f32_e32 v174, v174
	v_exp_f32_e32 v175, v175
	v_exp_f32_e32 v176, v176
	v_exp_f32_e32 v177, v177
	v_pk_add_f32 v[174:175], v[174:175], 1.0 op_sel_hi:[1,0]
	v_pk_add_f32 v[176:177], v[176:177], 1.0 op_sel_hi:[1,0]
	v_rcp_f32_e32 v174, v174
	v_rcp_f32_e32 v175, v175
	v_rcp_f32_e32 v176, v176
	v_rcp_f32_e32 v177, v177
	v_pk_fma_f32 v[248:249], v[174:175], v[122:123], v[248:249]
	v_pk_fma_f32 v[248:249], v[176:177], v[124:125], v[248:249]
	v_add_f32_e32 v114, v248, v249
	ds_bpermute_b32 v106, v206, v114
	s_waitcnt vmcnt(14)
	v_cmp_eq_u32_e64 s[0:1], 0, v210
	s_waitcnt lgkmcnt(0)
	v_add_f32_e32 v106, v114, v106
	ds_bpermute_b32 v107, v205, v106
	s_waitcnt lgkmcnt(0)
	v_add_f32_e32 v106, v106, v107
	v_add_f32_e32 v106, v212, v106
	v_mul_f32_e32 v106, 0x3fb8aa3b, v106
	v_exp_f32_e32 v106, v106
	s_nop 0
	v_cndmask_b32_e64 v106, 0, v106, s[0:1]
	s_and_saveexec_b64 s[0:1], vcc
	s_cbranch_execz .LBB1_18
	global_store_dword v[198:199], v106, off offset:128

.Lpf_2_b:
	s_add_u32 s100, s22, s32
	s_addc_u32 s101, s90, 0
	s_add_u32 s100, s100, 0xa0100
	s_addc_u32 s101, s101, 0
	global_load_dwordx4 v[136:139], v201, s[100:101] nt
	s_add_u32 s100, s22, s32
	s_addc_u32 s101, s90, 0
	s_add_u32 s100, s100, 0xc0100
	s_addc_u32 s101, s101, 0
	global_load_dwordx4 v[148:151], v201, s[100:101] nt
	s_add_u32 s100, s22, s32
	s_addc_u32 s101, s90, 0
	s_add_u32 s100, s100, 0xe0100
	s_addc_u32 s101, s101, 0
	global_load_dwordx4 v[160:163], v201, s[100:101] nt
	v_exp_f32_e32 v66, v66
	v_exp_f32_e32 v67, v67
	v_exp_f32_e32 v68, v68
	v_exp_f32_e32 v69, v69
	v_pk_add_f32 v[66:67], v[66:67], 1.0 op_sel_hi:[1,0]
	v_pk_add_f32 v[68:69], v[68:69], 1.0 op_sel_hi:[1,0]
	v_rcp_f32_e32 v66, v66
	v_rcp_f32_e32 v67, v67
	v_rcp_f32_e32 v68, v68
	v_rcp_f32_e32 v69, v69
	v_pk_mul_f32 v[248:249], v[66:67], v[102:103]
	v_pk_fma_f32 v[248:249], v[68:69], v[104:105], v[248:249]
	v_exp_f32_e32 v70, v70
	v_exp_f32_e32 v71, v71
	v_exp_f32_e32 v72, v72
	v_exp_f32_e32 v73, v73
	v_pk_add_f32 v[70:71], v[70:71], 1.0 op_sel_hi:[1,0]
	v_pk_add_f32 v[72:73], v[72:73], 1.0 op_sel_hi:[1,0]
	v_rcp_f32_e32 v70, v70
	v_rcp_f32_e32 v71, v71
	v_rcp_f32_e32 v72, v72
	v_rcp_f32_e32 v73, v73
	v_pk_fma_f32 v[248:249], v[70:71], v[90:91], v[248:249]
	v_pk_fma_f32 v[248:249], v[72:73], v[92:93], v[248:249]
	v_exp_f32_e32 v74, v74
	v_exp_f32_e32 v75, v75
	v_exp_f32_e32 v76, v76
	v_exp_f32_e32 v77, v77
	v_pk_add_f32 v[74:75], v[74:75], 1.0 op_sel_hi:[1,0]
	v_pk_add_f32 v[76:77], v[76:77], 1.0 op_sel_hi:[1,0]
	v_rcp_f32_e32 v74, v74
	v_rcp_f32_e32 v75, v75
	v_rcp_f32_e32 v76, v76
	v_rcp_f32_e32 v77, v77
	v_pk_fma_f32 v[248:249], v[74:75], v[98:99], v[248:249]
	v_pk_fma_f32 v[248:249], v[76:77], v[100:101], v[248:249]
	v_exp_f32_e32 v78, v78
	v_exp_f32_e32 v79, v79
	v_exp_f32_e32 v80, v80
	v_exp_f32_e32 v81, v81
	v_pk_add_f32 v[78:79], v[78:79], 1.0 op_sel_hi:[1,0]
	v_pk_add_f32 v[80:81], v[80:81], 1.0 op_sel_hi:[1,0]
	v_rcp_f32_e32 v78, v78
	v_rcp_f32_e32 v79, v79
	v_rcp_f32_e32 v80, v80
	v_rcp_f32_e32 v81, v81
	v_pk_fma_f32 v[248:249], v[78:79], v[86:87], v[248:249]
	v_pk_fma_f32 v[248:249], v[80:81], v[88:89], v[248:249]
	v_exp_f32_e32 v82, v82
	v_exp_f32_e32 v83, v83
	v_exp_f32_e32 v84, v84
	v_exp_f32_e32 v85, v85
	v_pk_add_f32 v[82:83], v[82:83], 1.0 op_sel_hi:[1,0]
	v_pk_add_f32 v[84:85], v[84:85], 1.0 op_sel_hi:[1,0]
	v_rcp_f32_e32 v82, v82
	v_rcp_f32_e32 v83, v83
	v_rcp_f32_e32 v84, v84
	v_rcp_f32_e32 v85, v85
	v_pk_fma_f32 v[248:249], v[82:83], v[118:119], v[248:249]
	v_pk_fma_f32 v[248:249], v[84:85], v[120:121], v[248:249]
	v_exp_f32_e32 v94, v94
	v_exp_f32_e32 v95, v95
	v_exp_f32_e32 v96, v96
	v_exp_f32_e32 v97, v97
	v_pk_add_f32 v[94:95], v[94:95], 1.0 op_sel_hi:[1,0]
	v_pk_add_f32 v[96:97], v[96:97], 1.0 op_sel_hi:[1,0]
	v_rcp_f32_e32 v94, v94
	v_rcp_f32_e32 v95, v95
	v_rcp_f32_e32 v96, v96
	v_rcp_f32_e32 v97, v97
	v_pk_fma_f32 v[248:249], v[94:95], v[110:111], v[248:249]
	v_pk_fma_f32 v[248:249], v[96:97], v[112:113], v[248:249]
	v_exp_f32_e32 v130, v130
	v_exp_f32_e32 v131, v131
	v_exp_f32_e32 v132, v132
	v_exp_f32_e32 v133, v133
	v_pk_add_f32 v[130:131], v[130:131], 1.0 op_sel_hi:[1,0]
	v_pk_add_f32 v[132:133], v[132:133], 1.0 op_sel_hi:[1,0]
	v_rcp_f32_e32 v130, v130
	v_rcp_f32_e32 v131, v131
	v_rcp_f32_e32 v132, v132
	v_rcp_f32_e32 v133, v133
	v_pk_fma_f32 v[248:249], v[130:131], v[126:127], v[248:249]
	v_pk_fma_f32 v[248:249], v[132:133], v[128:129], v[248:249]
	v_exp_f32_e32 v142, v142
	v_exp_f32_e32 v143, v143
	v_exp_f32_e32 v144, v144
	v_exp_f32_e32 v145, v145
	v_pk_add_f32 v[142:143], v[142:143], 1.0 op_sel_hi:[1,0]
	v_pk_add_f32 v[144:145], v[144:145], 1.0 op_sel_hi:[1,0]
	v_rcp_f32_e32 v142, v142
	v_rcp_f32_e32 v143, v143
	v_rcp_f32_e32 v144, v144
	v_rcp_f32_e32 v145, v145
	v_pk_fma_f32 v[248:249], v[142:143], v[122:123], v[248:249]
	v_pk_fma_f32 v[248:249], v[144:145], v[124:125], v[248:249]
	v_add_f32_e32 v66, v248, v249
	ds_bpermute_b32 v67, v206, v66
	s_waitcnt vmcnt(16)
	v_cmp_eq_u32_e64 s[0:1], 0, v209
	s_waitcnt lgkmcnt(0)
	v_add_f32_e32 v66, v66, v67
	ds_bpermute_b32 v67, v205, v66
	s_waitcnt lgkmcnt(0)
	v_add_f32_e32 v66, v66, v67
	v_add_f32_e32 v66, v212, v66
	v_mul_f32_e32 v66, 0x3fb8aa3b, v66
	v_exp_f32_e32 v66, v66
	s_nop 0
	v_cndmask_b32_e64 v66, 0, v66, s[0:1]
	s_and_saveexec_b64 s[0:1], vcc
	s_cbranch_execz .LBB1_20
	global_store_dword v[198:199], v66, off offset:192
.LBB1_20:
	s_or_b64 exec, exec, s[0:1]
	s_setprio 0
	v_add_f32_e32 v67, v194, v154
	v_add_f32_e32 v67, v67, v106
	v_add_f32_e32 v67, v67, v66
	v_mov_b32_e32 v69, v195
	v_cmp_eq_u32_e32 vcc, 0, v204
	v_add_f32_dpp v67, v67, v67 quad_perm:[1,0,3,2] row_mask:0xf bank_mask:0xf bound_ctrl:1
	s_nop 1
	v_add_f32_dpp v67, v67, v67 quad_perm:[2,3,0,1] row_mask:0xf bank_mask:0xf bound_ctrl:1
	s_nop 1
	v_add_f32_dpp v68, v67, v67 row_half_mirror row_mask:0xf bank_mask:0xf bound_ctrl:1
	v_lshl_or_b32 v67, v208, 2, v207
	v_mul_lo_u32 v67, v67, s85
	v_mov_b32_dpp v69, v68 row_mirror row_mask:0xf bank_mask:0xf
	s_and_saveexec_b64 s[0:1], vcc
	v_add_f32_e32 v68, v68, v69
	ds_write_b32 v67, v68 offset:37376
	s_or_b64 exec, exec, s[0:1]
	v_lshl_add_u32 v68, v1, 12, v200
	v_and_b32_e32 v69, 51, v0
	v_lshl_or_b32 v70, v69, 2, v68
	v_and_b32_e32 v69, 48, v0
	v_lshl_add_u32 v67, v69, 2, v67
	v_lshlrev_b32_e32 v69, 4, v0
	v_and_b32_e32 v69, 48, v69
	v_and_b32_e32 v71, 12, v0
	v_add3_u32 v67, v67, v69, v71
	v_cvt_f32_f16_e32 v69, v50
	v_cvt_f32_f16_sdwa v50, v50 dst_sel:DWORD dst_unused:UNUSED_PAD src0_sel:WORD_1
	v_lshl_or_b32 v68, v204, 6, v68
	s_and_b64 s[0:1], exec, s[72:73]
	v_mul_f32_e32 v69, v194, v69
	v_mul_f32_e32 v50, v194, v50
	v_fma_mix_f32 v50, v154, v54, v50 op_sel:[0,1,0] op_sel_hi:[0,1,0]
	v_fma_mix_f32 v50, v106, v58, v50 op_sel:[0,1,0] op_sel_hi:[0,1,0]
	v_fma_mix_f32 v69, v154, v54, v69 op_sel_hi:[0,1,0]
	v_fma_mix_f32 v54, v66, v62, v50 op_sel:[0,1,0] op_sel_hi:[0,1,0]
	v_bitop3_b32 v50, v0, 4, 12 bitop3:0x6c
	v_lshl_or_b32 v50, v50, 2, v70
	ds_write_b32 v50, v54 offset:256
	v_cvt_f32_f16_e32 v54, v51
	v_cvt_f32_f16_sdwa v51, v51 dst_sel:DWORD dst_unused:UNUSED_PAD src0_sel:WORD_1
	v_fma_mix_f32 v69, v106, v58, v69 op_sel_hi:[0,1,0]
	v_fma_mix_f32 v72, v66, v62, v69 op_sel_hi:[0,1,0]
	v_mul_f32_e32 v54, v194, v54
	v_mul_f32_e32 v51, v194, v51
	v_fma_mix_f32 v51, v154, v55, v51 op_sel:[0,1,0] op_sel_hi:[0,1,0]
	v_fma_mix_f32 v51, v106, v59, v51 op_sel:[0,1,0] op_sel_hi:[0,1,0]
	v_fma_mix_f32 v54, v154, v55, v54 op_sel_hi:[0,1,0]
	v_fma_mix_f32 v55, v66, v63, v51 op_sel:[0,1,0] op_sel_hi:[0,1,0]
	v_bitop3_b32 v51, v0, 12, v0 bitop3:0xc
	v_lshl_or_b32 v51, v51, 2, v70
	ds_write_b32 v51, v55 offset:768
	v_cvt_f32_f16_e32 v55, v52
	v_cvt_f32_f16_sdwa v52, v52 dst_sel:DWORD dst_unused:UNUSED_PAD src0_sel:WORD_1
	v_fma_mix_f32 v54, v106, v59, v54 op_sel_hi:[0,1,0]
	v_fma_mix_f32 v58, v66, v63, v54 op_sel_hi:[0,1,0]
	v_bitop3_b32 v54, v0, 8, 12 bitop3:0x6c
	v_mul_f32_e32 v52, v194, v52
	v_fma_mix_f32 v52, v154, v56, v52 op_sel:[0,1,0] op_sel_hi:[0,1,0]
	v_fma_mix_f32 v52, v106, v60, v52 op_sel:[0,1,0] op_sel_hi:[0,1,0]
	v_fma_mix_f32 v52, v66, v64, v52 op_sel:[0,1,0] op_sel_hi:[0,1,0]
	ds_write_b32 v50, v52 offset:1280
	v_cvt_f32_f16_e32 v52, v53
	v_lshl_or_b32 v54, v54, 2, v70
	v_lshl_or_b32 v69, v71, 2, v70
	v_mul_f32_e32 v55, v194, v55
	v_mul_f32_e32 v52, v194, v52
	v_fma_mix_f32 v52, v154, v57, v52 op_sel_hi:[0,1,0]
	v_fma_mix_f32 v52, v106, v61, v52 op_sel_hi:[0,1,0]
	v_fma_mix_f32 v52, v66, v65, v52 op_sel_hi:[0,1,0]
	ds_write_b32 v54, v52 offset:1536
	v_cvt_f32_f16_sdwa v52, v53 dst_sel:DWORD dst_unused:UNUSED_PAD src0_sel:WORD_1
	v_fma_mix_f32 v55, v154, v56, v55 op_sel_hi:[0,1,0]
	v_fma_mix_f32 v55, v106, v60, v55 op_sel_hi:[0,1,0]
	v_fma_mix_f32 v55, v66, v64, v55 op_sel_hi:[0,1,0]
	v_mul_f32_e32 v52, v194, v52
	v_fma_mix_f32 v52, v154, v57, v52 op_sel:[0,1,0] op_sel_hi:[0,1,0]
	v_fma_mix_f32 v52, v106, v61, v52 op_sel:[0,1,0] op_sel_hi:[0,1,0]
	v_fma_mix_f32 v52, v66, v65, v52 op_sel:[0,1,0] op_sel_hi:[0,1,0]
	ds_write_b32 v51, v52 offset:1792
	v_cvt_f32_f16_e32 v52, v34
	v_cvt_f32_f16_sdwa v34, v34 dst_sel:DWORD dst_unused:UNUSED_PAD src0_sel:WORD_1
	ds_write_b32 v69, v72
	ds_write_b32 v54, v58 offset:512
	v_mul_f32_e32 v52, v194, v52
	v_mul_f32_e32 v34, v194, v34
	v_fma_mix_f32 v34, v154, v38, v34 op_sel:[0,1,0] op_sel_hi:[0,1,0]
	v_fma_mix_f32 v34, v106, v42, v34 op_sel:[0,1,0] op_sel_hi:[0,1,0]
	v_fma_mix_f32 v34, v66, v46, v34 op_sel:[0,1,0] op_sel_hi:[0,1,0]
	ds_write_b32 v50, v34 offset:2304
	v_cvt_f32_f16_e32 v34, v35
	v_fma_mix_f32 v52, v154, v38, v52 op_sel_hi:[0,1,0]
	v_fma_mix_f32 v52, v106, v42, v52 op_sel_hi:[0,1,0]
	v_fma_mix_f32 v52, v66, v46, v52 op_sel_hi:[0,1,0]
	v_mul_f32_e32 v34, v194, v34
	v_fma_mix_f32 v34, v154, v39, v34 op_sel_hi:[0,1,0]
	v_fma_mix_f32 v34, v106, v43, v34 op_sel_hi:[0,1,0]
	v_fma_mix_f32 v34, v66, v47, v34 op_sel_hi:[0,1,0]
	ds_write_b32 v54, v34 offset:2560
	v_cvt_f32_f16_sdwa v34, v35 dst_sel:DWORD dst_unused:UNUSED_PAD src0_sel:WORD_1
	ds_write_b32 v69, v55 offset:1024
	ds_write_b32 v69, v52 offset:2048
	s_cselect_b32 s0, 0, 8
	v_mul_f32_e32 v34, v194, v34
	v_fma_mix_f32 v34, v154, v39, v34 op_sel:[0,1,0] op_sel_hi:[0,1,0]
	v_fma_mix_f32 v34, v106, v43, v34 op_sel:[0,1,0] op_sel_hi:[0,1,0]
	v_fma_mix_f32 v34, v66, v47, v34 op_sel:[0,1,0] op_sel_hi:[0,1,0]
	ds_write_b32 v51, v34 offset:2816
	v_cvt_f32_f16_e32 v34, v36
	s_add_i32 s22, s0, s89
	s_lshl_b64 s[0:1], s[22:23], 20
	s_add_u32 s0, s6, s0
	v_mul_f32_e32 v34, v194, v34
	v_fma_mix_f32 v34, v154, v40, v34 op_sel_hi:[0,1,0]
	v_fma_mix_f32 v34, v106, v44, v34 op_sel_hi:[0,1,0]
	v_fma_mix_f32 v34, v66, v48, v34 op_sel_hi:[0,1,0]
	ds_write_b32 v69, v34 offset:3072
	v_cvt_f32_f16_sdwa v34, v36 dst_sel:DWORD dst_unused:UNUSED_PAD src0_sel:WORD_1
	s_addc_u32 s1, s7, s1
	s_mov_b64 s[72:73], s[0:1]
	v_mul_f32_e32 v34, v194, v34
	v_fma_mix_f32 v34, v154, v40, v34 op_sel:[0,1,0] op_sel_hi:[0,1,0]
	v_fma_mix_f32 v34, v106, v44, v34 op_sel:[0,1,0] op_sel_hi:[0,1,0]
	v_fma_mix_f32 v34, v66, v48, v34 op_sel:[0,1,0] op_sel_hi:[0,1,0]
	ds_write_b32 v50, v34 offset:3328
	v_cvt_f32_f16_e32 v34, v37
	v_mul_f32_e32 v34, v194, v34
	v_fma_mix_f32 v34, v154, v41, v34 op_sel_hi:[0,1,0]
	v_fma_mix_f32 v34, v106, v45, v34 op_sel_hi:[0,1,0]
	v_fma_mix_f32 v34, v66, v49, v34 op_sel_hi:[0,1,0]
	ds_write_b32 v54, v34 offset:3584
	v_cvt_f32_f16_sdwa v34, v37 dst_sel:DWORD dst_unused:UNUSED_PAD src0_sel:WORD_1
	v_mul_f32_e32 v34, v194, v34
	v_fma_mix_f32 v34, v154, v41, v34 op_sel:[0,1,0] op_sel_hi:[0,1,0]
	v_fma_mix_f32 v34, v106, v45, v34 op_sel:[0,1,0] op_sel_hi:[0,1,0]
	v_fma_mix_f32 v34, v66, v49, v34 op_sel:[0,1,0] op_sel_hi:[0,1,0]
	ds_write_b32 v51, v34 offset:3840
	ds_read_b128 v[34:37], v68
	ds_read_b128 v[38:41], v68 offset:16
	ds_read_b128 v[42:45], v68 offset:32
	ds_read_b128 v[46:49], v68 offset:48
	s_waitcnt lgkmcnt(2)
	v_pk_add_f32 v[36:37], v[36:37], v[40:41]
	v_pk_add_f32 v[34:35], v[34:35], v[38:39]
	s_waitcnt lgkmcnt(0)
	v_pk_add_f32 v[38:39], v[44:45], v[48:49]
	v_pk_add_f32 v[40:41], v[42:43], v[46:47]
	v_pk_add_f32 v[36:37], v[36:37], v[38:39]
	v_pk_add_f32 v[34:35], v[34:35], v[40:41]
	s_nop 0
	v_add_f32_e32 v34, v34, v35
	v_add_f32_e32 v35, v36, v37
	v_add_f32_e32 v34, v34, v35
	ds_write_b32 v67, v34 offset:36864
	v_cvt_f32_f16_e32 v34, v2
	v_cvt_f32_f16_sdwa v2, v2 dst_sel:DWORD dst_unused:UNUSED_PAD src0_sel:WORD_1
	v_mul_f32_e32 v34, v194, v34
	v_mul_f32_e32 v2, v194, v2
	v_fma_mix_f32 v2, v154, v6, v2 op_sel:[0,1,0] op_sel_hi:[0,1,0]
	v_fma_mix_f32 v2, v106, v14, v2 op_sel:[0,1,0] op_sel_hi:[0,1,0]
	v_fma_mix_f32 v2, v66, v30, v2 op_sel:[0,1,0] op_sel_hi:[0,1,0]
	ds_write_b32 v50, v2 offset:256
	v_cvt_f32_f16_e32 v2, v3
	v_fma_mix_f32 v34, v154, v6, v34 op_sel_hi:[0,1,0]
	v_fma_mix_f32 v34, v106, v14, v34 op_sel_hi:[0,1,0]
	v_fma_mix_f32 v34, v66, v30, v34 op_sel_hi:[0,1,0]
	v_mul_f32_e32 v2, v194, v2
	v_fma_mix_f32 v2, v154, v7, v2 op_sel_hi:[0,1,0]
	v_fma_mix_f32 v2, v106, v15, v2 op_sel_hi:[0,1,0]
	v_fma_mix_f32 v2, v66, v31, v2 op_sel_hi:[0,1,0]
	ds_write_b32 v54, v2 offset:512
	v_cvt_f32_f16_sdwa v2, v3 dst_sel:DWORD dst_unused:UNUSED_PAD src0_sel:WORD_1
	ds_write_b32 v69, v34
	v_mul_f32_e32 v2, v194, v2
	v_fma_mix_f32 v2, v154, v7, v2 op_sel:[0,1,0] op_sel_hi:[0,1,0]
	v_fma_mix_f32 v2, v106, v15, v2 op_sel:[0,1,0] op_sel_hi:[0,1,0]
	v_fma_mix_f32 v2, v66, v31, v2 op_sel:[0,1,0] op_sel_hi:[0,1,0]
	ds_write_b32 v51, v2 offset:768
	v_cvt_f32_f16_e32 v2, v4
	v_mul_f32_e32 v2, v194, v2
	v_fma_mix_f32 v2, v154, v8, v2 op_sel_hi:[0,1,0]
	v_fma_mix_f32 v2, v106, v16, v2 op_sel_hi:[0,1,0]
	v_fma_mix_f32 v2, v66, v32, v2 op_sel_hi:[0,1,0]
	ds_write_b32 v69, v2 offset:1024
	v_cvt_f32_f16_sdwa v2, v4 dst_sel:DWORD dst_unused:UNUSED_PAD src0_sel:WORD_1
	v_mul_f32_e32 v2, v194, v2
	v_fma_mix_f32 v2, v154, v8, v2 op_sel:[0,1,0] op_sel_hi:[0,1,0]
	v_fma_mix_f32 v2, v106, v16, v2 op_sel:[0,1,0] op_sel_hi:[0,1,0]
	v_fma_mix_f32 v2, v66, v32, v2 op_sel:[0,1,0] op_sel_hi:[0,1,0]
	ds_write_b32 v50, v2 offset:1280
	v_cvt_f32_f16_e32 v2, v5
	v_mul_f32_e32 v2, v194, v2
	v_fma_mix_f32 v2, v154, v9, v2 op_sel_hi:[0,1,0]
	v_fma_mix_f32 v2, v106, v17, v2 op_sel_hi:[0,1,0]
	v_fma_mix_f32 v2, v66, v33, v2 op_sel_hi:[0,1,0]
	ds_write_b32 v54, v2 offset:1536
	v_cvt_f32_f16_sdwa v2, v5 dst_sel:DWORD dst_unused:UNUSED_PAD src0_sel:WORD_1
	v_mul_f32_e32 v2, v194, v2
	v_fma_mix_f32 v2, v154, v9, v2 op_sel:[0,1,0] op_sel_hi:[0,1,0]
	v_fma_mix_f32 v2, v106, v17, v2 op_sel:[0,1,0] op_sel_hi:[0,1,0]
	v_fma_mix_f32 v2, v66, v33, v2 op_sel:[0,1,0] op_sel_hi:[0,1,0]
	ds_write_b32 v51, v2 offset:1792
	v_cvt_f32_f16_e32 v2, v10
	v_mul_f32_e32 v2, v194, v2
	v_fma_mix_f32 v2, v154, v18, v2 op_sel_hi:[0,1,0]
	v_fma_mix_f32 v2, v106, v22, v2 op_sel_hi:[0,1,0]
	v_fma_mix_f32 v2, v66, v26, v2 op_sel_hi:[0,1,0]
	ds_write_b32 v69, v2 offset:2048
	v_cvt_f32_f16_sdwa v2, v10 dst_sel:DWORD dst_unused:UNUSED_PAD src0_sel:WORD_1
	v_mul_f32_e32 v2, v194, v2
	v_fma_mix_f32 v2, v154, v18, v2 op_sel:[0,1,0] op_sel_hi:[0,1,0]
	v_fma_mix_f32 v2, v106, v22, v2 op_sel:[0,1,0] op_sel_hi:[0,1,0]
	v_fma_mix_f32 v2, v66, v26, v2 op_sel:[0,1,0] op_sel_hi:[0,1,0]
	ds_write_b32 v50, v2 offset:2304
	v_cvt_f32_f16_e32 v2, v11
	v_mul_f32_e32 v2, v194, v2
	v_fma_mix_f32 v2, v154, v19, v2 op_sel_hi:[0,1,0]
	v_fma_mix_f32 v2, v106, v23, v2 op_sel_hi:[0,1,0]
	v_fma_mix_f32 v2, v66, v27, v2 op_sel_hi:[0,1,0]
	ds_write_b32 v54, v2 offset:2560
	v_cvt_f32_f16_sdwa v2, v11 dst_sel:DWORD dst_unused:UNUSED_PAD src0_sel:WORD_1
	v_mul_f32_e32 v2, v194, v2
	v_fma_mix_f32 v2, v154, v19, v2 op_sel:[0,1,0] op_sel_hi:[0,1,0]
	v_fma_mix_f32 v2, v106, v23, v2 op_sel:[0,1,0] op_sel_hi:[0,1,0]
	v_fma_mix_f32 v2, v66, v27, v2 op_sel:[0,1,0] op_sel_hi:[0,1,0]
	ds_write_b32 v51, v2 offset:2816
	v_cvt_f32_f16_e32 v2, v12
	v_mul_f32_e32 v2, v194, v2
	v_fma_mix_f32 v2, v154, v20, v2 op_sel_hi:[0,1,0]
	v_fma_mix_f32 v2, v106, v24, v2 op_sel_hi:[0,1,0]
	v_fma_mix_f32 v2, v66, v28, v2 op_sel_hi:[0,1,0]
	ds_write_b32 v69, v2 offset:3072
	v_cvt_f32_f16_sdwa v2, v12 dst_sel:DWORD dst_unused:UNUSED_PAD src0_sel:WORD_1
	v_mul_f32_e32 v2, v194, v2
	v_fma_mix_f32 v2, v154, v20, v2 op_sel:[0,1,0] op_sel_hi:[0,1,0]
	v_fma_mix_f32 v2, v106, v24, v2 op_sel:[0,1,0] op_sel_hi:[0,1,0]
	v_fma_mix_f32 v2, v66, v28, v2 op_sel:[0,1,0] op_sel_hi:[0,1,0]
	ds_write_b32 v50, v2 offset:3328
	v_cvt_f32_f16_e32 v2, v13
	v_mul_f32_e32 v2, v194, v2
	v_fma_mix_f32 v2, v154, v21, v2 op_sel_hi:[0,1,0]
	v_fma_mix_f32 v2, v106, v25, v2 op_sel_hi:[0,1,0]
	v_fma_mix_f32 v2, v66, v29, v2 op_sel_hi:[0,1,0]
	ds_write_b32 v54, v2 offset:3584
	v_cvt_f32_f16_sdwa v2, v13 dst_sel:DWORD dst_unused:UNUSED_PAD src0_sel:WORD_1
	v_mul_f32_e32 v2, v194, v2
	v_fma_mix_f32 v2, v154, v21, v2 op_sel:[0,1,0] op_sel_hi:[0,1,0]
	v_fma_mix_f32 v2, v106, v25, v2 op_sel:[0,1,0] op_sel_hi:[0,1,0]
	v_fma_mix_f32 v2, v66, v29, v2 op_sel:[0,1,0] op_sel_hi:[0,1,0]
	ds_write_b32 v51, v2 offset:3840
	ds_read_b128 v[2:5], v68
	ds_read_b128 v[6:9], v68 offset:16
	ds_read_b128 v[10:13], v68 offset:32
	ds_read_b128 v[14:17], v68 offset:48
	s_waitcnt lgkmcnt(2)
	v_pk_add_f32 v[4:5], v[4:5], v[8:9]
	v_pk_add_f32 v[2:3], v[2:3], v[6:7]
	s_waitcnt lgkmcnt(0)
	v_pk_add_f32 v[6:7], v[12:13], v[16:17]
	v_pk_add_f32 v[8:9], v[10:11], v[14:15]
	v_pk_add_f32 v[4:5], v[4:5], v[6:7]
	v_pk_add_f32 v[2:3], v[2:3], v[8:9]
	s_nop 0
	v_add_f32_e32 v2, v2, v3
	v_add_f32_e32 v3, v4, v5
	v_add_f32_e32 v2, v2, v3
	ds_write_b32 v67, v2 offset:37120
	s_waitcnt vmcnt(0)
	s_add_u32 s80, s72, 0x20000
	s_addc_u32 s81, s73, 0
	s_add_u32 s90, s72, 0x40000
	s_addc_u32 s91, s73, 0
	s_add_u32 s92, s72, 0x60000
	s_addc_u32 s93, s73, 0
	s_add_u32 s94, s72, 0x80000
	s_addc_u32 s95, s73, 0
	s_add_u32 s96, s72, 0xa0000
	s_addc_u32 s97, s73, 0
	s_add_u32 s98, s72, 0xc0000
	s_addc_u32 s99, s73, 0
	s_add_u32 s64, s72, 0xe0000
	s_addc_u32 s65, s73, 0
	s_add_u32 s0, s0, 0x100
	s_addc_u32 s1, s1, 0
	v_mov_b64_e32 v[62:63], v[216:217]
	v_mov_b64_e32 v[64:65], v[218:219]
	v_mov_b64_e32 v[58:59], v[220:221]
	v_mov_b64_e32 v[60:61], v[222:223]
	v_mov_b64_e32 v[54:55], v[224:225]
	v_mov_b64_e32 v[56:57], v[226:227]
	v_mov_b64_e32 v[50:51], v[228:229]
	v_mov_b64_e32 v[52:53], v[230:231]
	v_mov_b64_e32 v[46:47], v[232:233]
	v_mov_b64_e32 v[48:49], v[234:235]
	v_mov_b64_e32 v[42:43], v[236:237]
	v_mov_b64_e32 v[44:45], v[238:239]
	v_mov_b64_e32 v[38:39], v[240:241]
	v_mov_b64_e32 v[40:41], v[242:243]
	v_mov_b64_e32 v[34:35], v[244:245]
	v_mov_b64_e32 v[36:37], v[246:247]
	s_add_u32 s64, s0, 0x20000
	s_addc_u32 s65, s1, 0
	s_add_u32 s72, s0, 0x40000
	s_addc_u32 s73, s1, 0
	s_add_u32 s80, s0, 0x60000
	s_addc_u32 s81, s1, 0
	s_add_u32 s90, s0, 0x80000
	s_addc_u32 s91, s1, 0
	s_add_u32 s92, s0, 0xa0000
	s_addc_u32 s93, s1, 0
	s_add_u32 s94, s0, 0xc0000
	s_addc_u32 s95, s1, 0
	s_add_u32 s96, s0, 0xe0000
	s_addc_u32 s97, s1, 0
	v_mov_b64_e32 v[30:31], v[156:157]
	v_mov_b64_e32 v[32:33], v[158:159]
	v_mov_b64_e32 v[26:27], v[168:169]
	v_mov_b64_e32 v[28:29], v[170:171]
	v_mov_b64_e32 v[22:23], v[180:181]
	v_mov_b64_e32 v[24:25], v[182:183]
	v_mov_b64_e32 v[18:19], v[184:185]
	v_mov_b64_e32 v[20:21], v[186:187]
	v_mov_b64_e32 v[14:15], v[188:189]
	v_mov_b64_e32 v[16:17], v[190:191]
	v_mov_b64_e32 v[10:11], v[136:137]
	v_mov_b64_e32 v[12:13], v[138:139]
	v_mov_b64_e32 v[6:7], v[148:149]
	v_mov_b64_e32 v[8:9], v[150:151]
	v_mov_b64_e32 v[2:3], v[160:161]
	v_mov_b64_e32 v[4:5], v[162:163]
	s_andn2_b64 vcc, exec, s[70:71]
	s_waitcnt lgkmcnt(0)
	s_barrier
	s_cbranch_vccnz .LBB1_24
	v_lshlrev_b32_e32 v1, 10, v1
	v_add_u32_e32 v70, 0x2000, v1
	v_readfirstlane_b32 s0, v1
	v_lshl_add_u64 v[66:67], s[4:5], 0, v[196:197]
	s_mov_b32 m0, s0
	v_readfirstlane_b32 s0, v70
	v_add_u32_e32 v70, 0x4000, v1
	global_load_lds_dwordx4 v[66:67], off
	v_lshl_add_u64 v[68:69], v[66:67], 0, s[58:59]
	s_mov_b32 m0, s0
	v_readfirstlane_b32 s0, v70
	v_add_u32_e32 v1, 0x6000, v1
	global_load_lds_dwordx4 v[68:69], off
	v_lshl_add_u64 v[68:69], v[66:67], 0, s[60:61]
	s_mov_b32 m0, s0
	v_readfirstlane_b32 s0, v1
	global_load_lds_dwordx4 v[68:69], off
	v_lshl_add_u64 v[66:67], v[66:67], 0, s[62:63]
	s_mov_b32 m0, s0
	s_nop 0
	global_load_lds_dwordx4 v[66:67], off
